# P1 conversion share made uniform (160 items per workgroup, even count per wave); queue-grab store drain removed
# baseline (speedup 1.0000x reference)
.LBB0_136:
	s_or_b64 exec, exec, s[4:5]
	s_cmp_lt_i32 s94, 2
	s_cselect_b64 s[0:1], -1, 0
	s_and_b64 s[22:23], s[0:1], s[6:7]
	s_andn2_b64 vcc, exec, s[22:23]
	v_writelane_b32 v255, s96, 29
	s_cbranch_vccnz .LBB0_296
	s_cmp_lt_i32 s96, 32
	s_cselect_b64 s[24:25], -1, 0
	s_cmp_gt_i32 s96, 31
	s_cbranch_scc0 .LBB0_139
	s_mul_i32 s0, s96, 0xa0
	s_add_i32 s52, s0, 0
	s_movk_i32 s53, 0xa0
	s_cbranch_execz .LBB0_140
	s_branch .LBB0_141
.LBB0_139:
	s_movk_i32 s53, 0xa0
.LBB0_140:
	s_movk_i32 s53, 0xa0
	s_mul_i32 s52, s96, 0xa0

.LBB0_1050:
	s_nop 0
